# vq_main stores write-through (sc0 sc1) so the kernel boundary has no dirty L2 to flush
# speedup vs baseline: 1.0451x; 1.0317x over previous
.LBB0_93:
	s_or_b64 exec, exec, s[6:7]
	s_waitcnt lgkmcnt(0)
	ds_read_b128 v[194:197], v179
	ds_read_b128 v[198:201], v179 offset:32
	ds_read_b128 v[202:205], v179 offset:64
	v_add_u32_e32 v66, 0x20c40, v188
	ds_read_b32 v191, v66
	v_add_u32_e32 v66, 0x20c00, v188
	s_waitcnt lgkmcnt(3)
	v_mfma_f32_32x32x16_f16 v[68:83], v[98:101], v[194:197], v[2:17]
	ds_read_b32 v192, v66
	ds_read_b128 v[206:209], v179 offset:96
	s_and_b32 s0, s17, 1
	s_waitcnt lgkmcnt(2)
	v_lshlrev_b32_e32 v66, 4, v191
	v_and_or_b32 v66, v66, s28, v1
	v_lshlrev_b32_e32 v66, 4, v66
	global_load_dwordx4 v[162:165], v66, s[22:23]
	s_mulk_i32 s0, 0x1200
	v_mfma_f32_32x32x16_f16 v[68:83], v[102:105], v[198:201], v[68:83]
	v_mfma_f32_32x32x16_f16 v[68:83], v[106:109], v[202:205], v[68:83]
	s_waitcnt lgkmcnt(0)
	v_mfma_f32_32x32x16_f16 v[68:83], v[110:113], v[206:209], v[68:83]
	v_lshlrev_b32_e32 v66, 4, v192
	v_and_or_b32 v66, v66, s28, v1
	v_lshlrev_b32_e32 v66, 4, v66
	global_load_dwordx4 v[216:219], v66, s[22:23]
	s_nop 7
	v_and_b32_e32 v84, 0xffffffc0, v68
	v_and_or_b32 v85, v69, s16, 1
	v_and_or_b32 v86, v70, s16, 2
	v_and_or_b32 v87, v71, s16, 3
	v_and_or_b32 v88, v72, s16, 4
	v_and_or_b32 v89, v73, s16, 5
	v_and_or_b32 v90, v74, s16, 6
	v_and_or_b32 v91, v75, s16, 7
	v_and_or_b32 v92, v76, s16, 8
	v_and_or_b32 v93, v77, s16, 9
	v_and_or_b32 v94, v78, s16, 10
	v_and_or_b32 v95, v79, s16, 11
	v_and_or_b32 v96, v80, s16, 12
	v_and_or_b32 v97, v81, s16, 13
	v_mfma_f32_32x32x16_f16 v[66:81], v[114:117], v[194:197], v[18:33]
	v_med3_f32 v193, v84, v85, s25
	v_min3_f32 v84, v84, s25, v85
	v_med3_f32 v85, v84, v86, v87
	v_min3_f32 v84, v84, v86, v87
	v_med3_f32 v86, v84, v88, v89
	v_min3_f32 v84, v84, v88, v89
	v_min3_f32 v85, v193, s25, v85
	v_mfma_f32_32x32x16_f16 v[66:81], v[118:121], v[198:201], v[66:81]
	v_med3_f32 v87, v84, v90, v91
	v_min3_f32 v84, v84, v90, v91
	v_min3_f32 v85, v85, v86, v87
	v_med3_f32 v86, v84, v92, v93
	v_min3_f32 v84, v84, v92, v93
	v_med3_f32 v87, v84, v94, v95
	v_min3_f32 v84, v84, v94, v95
	v_mfma_f32_32x32x16_f16 v[66:81], v[122:125], v[202:205], v[66:81]
	v_and_or_b32 v82, v82, s16, 14
	v_and_or_b32 v83, v83, s16, 15
	v_min3_f32 v85, v85, v86, v87
	v_med3_f32 v86, v84, v96, v97
	v_min3_f32 v84, v84, v96, v97
	v_med3_f32 v87, v84, v82, v83
	v_min3_f32 v193, v84, v82, v83
	v_mfma_f32_32x32x16_f16 v[66:81], v[126:129], v[206:209], v[66:81]
	v_min3_f32 v210, v85, v86, v87
	v_mfma_f32_32x32x16_f16 v[82:97], v[130:133], v[194:197], v[34:49]
	s_nop 9
	v_and_or_b32 v66, v66, s16, 16
	v_and_or_b32 v67, v67, s16, 17
	v_and_or_b32 v68, v68, s16, 18
	v_and_or_b32 v69, v69, s16, 19
	v_med3_f32 v211, v193, v66, v67
	v_min3_f32 v66, v193, v66, v67
	v_and_or_b32 v70, v70, s16, 20
	v_and_or_b32 v71, v71, s16, 21
	v_med3_f32 v67, v66, v68, v69
	v_min3_f32 v66, v66, v68, v69
	v_and_or_b32 v72, v72, s16, 22
	v_and_or_b32 v73, v73, s16, 23
	v_med3_f32 v68, v66, v70, v71
	v_min3_f32 v66, v66, v70, v71
	v_and_or_b32 v74, v74, s16, 24
	v_and_or_b32 v75, v75, s16, 25
	v_min3_f32 v67, v210, v211, v67
	v_med3_f32 v69, v66, v72, v73
	v_min3_f32 v66, v66, v72, v73
	v_and_or_b32 v76, v76, s16, 26
	v_and_or_b32 v77, v77, s16, 27
	v_min3_f32 v67, v67, v68, v69
	v_med3_f32 v68, v66, v74, v75
	v_min3_f32 v66, v66, v74, v75
	v_and_or_b32 v78, v78, s16, 28
	v_and_or_b32 v79, v79, s16, 29
	v_med3_f32 v69, v66, v76, v77
	v_min3_f32 v66, v66, v76, v77
	v_and_or_b32 v80, v80, s16, 30
	v_and_or_b32 v81, v81, s16, 31
	v_min3_f32 v67, v67, v68, v69
	v_med3_f32 v68, v66, v78, v79
	v_min3_f32 v66, v66, v78, v79
	v_med3_f32 v69, v66, v80, v81
	v_mfma_f32_32x32x16_f16 v[82:97], v[134:137], v[198:201], v[82:97]
	v_min3_f32 v193, v66, v80, v81
	v_min3_f32 v210, v67, v68, v69
	v_mfma_f32_32x32x16_f16 v[66:81], v[146:149], v[194:197], v[50:65]
	v_mfma_f32_32x32x16_f16 v[82:97], v[138:141], v[202:205], v[82:97]
	v_mfma_f32_32x32x16_f16 v[66:81], v[150:153], v[198:201], v[66:81]
	v_mfma_f32_32x32x16_f16 v[82:97], v[142:145], v[206:209], v[82:97]
	v_mfma_f32_32x32x16_f16 v[66:81], v[154:157], v[202:205], v[66:81]
	s_nop 10
	v_and_or_b32 v82, v82, s16, 32
	v_and_or_b32 v83, v83, s16, 33
	v_and_or_b32 v84, v84, s16, 34
	v_and_or_b32 v85, v85, s16, 35
	v_med3_f32 v194, v193, v82, v83
	v_min3_f32 v82, v193, v82, v83
	v_and_or_b32 v86, v86, s16, 36
	v_mfma_f32_32x32x16_f16 v[66:81], v[158:161], v[206:209], v[66:81]
	v_and_or_b32 v87, v87, s16, 37
	v_med3_f32 v83, v82, v84, v85
	v_min3_f32 v82, v82, v84, v85
	v_and_or_b32 v88, v88, s16, 38
	v_and_or_b32 v89, v89, s16, 39
	v_med3_f32 v84, v82, v86, v87
	v_min3_f32 v82, v82, v86, v87
	v_and_or_b32 v90, v90, s16, 40
	v_and_or_b32 v91, v91, s16, 41
	v_min3_f32 v83, v210, v194, v83
	v_med3_f32 v85, v82, v88, v89
	v_min3_f32 v82, v82, v88, v89
	v_and_or_b32 v92, v92, s16, 42
	v_and_or_b32 v93, v93, s16, 43
	v_min3_f32 v83, v83, v84, v85
	v_med3_f32 v84, v82, v90, v91
	v_min3_f32 v82, v82, v90, v91
	v_and_or_b32 v94, v94, s16, 44
	v_and_or_b32 v95, v95, s16, 45
	v_med3_f32 v85, v82, v92, v93
	v_min3_f32 v82, v82, v92, v93
	v_and_or_b32 v96, v96, s16, 46
	v_and_or_b32 v97, v97, s16, 47
	v_min3_f32 v83, v83, v84, v85
	v_med3_f32 v84, v82, v94, v95
	v_min3_f32 v82, v82, v94, v95
	v_med3_f32 v85, v82, v96, v97
	v_min3_f32 v82, v82, v96, v97
	v_and_or_b32 v66, v66, s16, 48
	v_and_or_b32 v67, v67, s16, 49
	v_min3_f32 v83, v83, v84, v85
	v_and_or_b32 v68, v68, s16, 50
	v_and_or_b32 v69, v69, s16, 51
	v_med3_f32 v84, v82, v66, v67
	v_min3_f32 v66, v82, v66, v67
	v_and_or_b32 v70, v70, s16, 52
	v_and_or_b32 v71, v71, s16, 53
	v_med3_f32 v67, v66, v68, v69
	v_min3_f32 v66, v66, v68, v69
	v_and_or_b32 v72, v72, s16, 54
	v_and_or_b32 v73, v73, s16, 55
	v_med3_f32 v68, v66, v70, v71
	v_min3_f32 v66, v66, v70, v71
	v_and_or_b32 v74, v74, s16, 56
	v_and_or_b32 v75, v75, s16, 57
	v_min3_f32 v67, v83, v84, v67
	v_med3_f32 v69, v66, v72, v73
	v_min3_f32 v66, v66, v72, v73
	v_and_or_b32 v76, v76, s16, 58
	v_and_or_b32 v77, v77, s16, 59
	v_min3_f32 v67, v67, v68, v69
	v_med3_f32 v68, v66, v74, v75
	v_min3_f32 v66, v66, v74, v75
	v_and_or_b32 v78, v78, s16, 60
	v_and_or_b32 v79, v79, s16, 61
	v_med3_f32 v69, v66, v76, v77
	v_min3_f32 v66, v66, v76, v77
	v_and_or_b32 v80, v80, s16, 62
	v_or_b32_e32 v81, 63, v81
	v_min3_f32 v67, v67, v68, v69
	v_med3_f32 v68, v66, v78, v79
	v_min3_f32 v66, v66, v78, v79
	v_med3_f32 v69, v66, v80, v81
	v_min3_f32 v66, v66, v80, v81
	v_min3_f32 v67, v67, v68, v69
	v_add_u32_e32 v68, s0, v177
	v_cmp_lt_i32_e64 s[0:1], -1, v192
	ds_write_b64 v68, v[66:67]
	s_waitcnt vmcnt(0)
	s_and_saveexec_b64 s[6:7], s[0:1]
	s_cbranch_execz .LBB0_95
	s_and_b32 s0, s29, 3
	v_lshl_add_u32 v70, s0, 13, v175
	ds_read_b128 v[70:73], v70
	s_waitcnt lgkmcnt(0)
	v_pk_add_f32 v[66:67], v[216:217], v[70:71] neg_lo:[0,1] neg_hi:[0,1]
	v_pk_add_f32 v[74:75], v[218:219], v[72:73] neg_lo:[0,1] neg_hi:[0,1]
	v_pk_mul_f32 v[76:77], v[66:67], v[66:67]
	v_pk_add_f32 v[66:67], v[70:71], v[66:67]
	v_pk_add_f32 v[68:69], v[72:73], v[74:75]
	v_pk_mul_f32 v[70:71], v[74:75], v[74:75]
	global_store_dwordx4 v[168:169], v[66:69], off sc0 sc1
	s_nop 1
	v_add_f32_e32 v66, v76, v77
	v_add_f32_e32 v66, v66, v70
	v_add_f32_e32 v66, v66, v71
	v_add_f32_e32 v167, v167, v66
.LBB0_95:
	s_or_b64 exec, exec, s[6:7]
	v_cmp_lt_i32_e64 s[0:1], -1, v191
	s_and_saveexec_b64 s[6:7], s[0:1]
	s_cbranch_execz .LBB0_87
	s_and_b32 s0, s29, 3
	v_lshl_add_u32 v66, s0, 13, v174
	ds_read_b128 v[66:69], v66
	s_waitcnt lgkmcnt(0)
	v_pk_add_f32 v[70:71], v[162:163], v[66:67] neg_lo:[0,1] neg_hi:[0,1]
	v_pk_add_f32 v[72:73], v[164:165], v[68:69] neg_lo:[0,1] neg_hi:[0,1]
	v_pk_mul_f32 v[74:75], v[70:71], v[70:71]
	v_pk_add_f32 v[66:67], v[66:67], v[70:71]
	v_pk_add_f32 v[68:69], v[68:69], v[72:73]
	v_pk_mul_f32 v[70:71], v[72:73], v[72:73]
	global_store_dwordx4 v[170:171], v[66:69], off sc0 sc1
	s_nop 1
	v_add_f32_e32 v66, v74, v75
	v_add_f32_e32 v66, v66, v70
	v_add_f32_e32 v66, v66, v71
	v_add_f32_e32 v167, v167, v66
	s_branch .LBB0_87

.LBB0_102:
	s_or_b64 exec, exec, s[0:1]
	v_lshlrev_b32_e32 v71, 2, v183
	s_waitcnt lgkmcnt(0)
	v_or_b32_e32 v66, 0x213c0, v71
	ds_read_b32 v70, v66
	v_or_b32_e32 v71, 0x21380, v71
	s_movk_i32 s4, 0x3ff0
	ds_read_b32 v71, v71
	s_waitcnt lgkmcnt(1)
	v_lshlrev_b32_e32 v66, 4, v70
	v_and_or_b32 v66, v66, s4, v1
	v_lshlrev_b32_e32 v66, 4, v66
	global_load_dwordx4 v[66:69], v66, s[22:23]
	s_waitcnt lgkmcnt(0)
	v_cmp_lt_i32_e32 vcc, -1, v71
	s_and_saveexec_b64 s[0:1], vcc
	s_cbranch_execz .LBB0_104
	v_lshlrev_b32_e32 v71, 4, v71
	v_and_or_b32 v71, v71, s4, v1
	v_lshlrev_b32_e32 v71, 4, v71
	global_load_dwordx4 v[72:75], v71, s[22:23]
	ds_read_b128 v[76:79], v175 offset:24576
	v_or_b32_e32 v71, s24, v183
	s_mov_b32 s4, 0x1e000
	v_lshlrev_b32_e32 v71, 8, v71
	v_or3_b32 v71, v71, v178, s4
	s_waitcnt vmcnt(0) lgkmcnt(0)
	v_pk_add_f32 v[72:73], v[72:73], v[76:77] neg_lo:[0,1] neg_hi:[0,1]
	v_pk_add_f32 v[80:81], v[74:75], v[78:79] neg_lo:[0,1] neg_hi:[0,1]
	v_pk_mul_f32 v[82:83], v[72:73], v[72:73]
	v_pk_add_f32 v[72:73], v[76:77], v[72:73]
	v_pk_add_f32 v[74:75], v[78:79], v[80:81]
	v_pk_mul_f32 v[76:77], v[80:81], v[80:81]
	global_store_dwordx4 v71, v[72:75], s[12:13] sc0 sc1
	v_add_f32_e32 v71, v82, v83
	v_add_f32_e32 v71, v71, v76
	v_add_f32_e32 v71, v71, v77
	v_add_f32_e32 v167, v167, v71
.LBB0_104:
	s_or_b64 exec, exec, s[0:1]
	v_cmp_lt_i32_e32 vcc, -1, v70
	s_and_saveexec_b64 s[0:1], vcc
	s_cbranch_execz .LBB0_106
	ds_read_b128 v[70:73], v174 offset:24576
	v_or_b32_e32 v74, s24, v173
	s_mov_b32 s4, 0x1e000
	v_lshlrev_b32_e32 v74, 8, v74
	v_or3_b32 v78, v74, v178, s4
	s_waitcnt vmcnt(0) lgkmcnt(0)
	v_pk_add_f32 v[66:67], v[66:67], v[70:71] neg_lo:[0,1] neg_hi:[0,1]
	v_pk_add_f32 v[76:77], v[68:69], v[72:73] neg_lo:[0,1] neg_hi:[0,1]
	v_pk_mul_f32 v[74:75], v[66:67], v[66:67]
	v_pk_add_f32 v[66:67], v[70:71], v[66:67]
	v_pk_add_f32 v[68:69], v[72:73], v[76:77]
	global_store_dwordx4 v78, v[66:69], s[12:13] sc0 sc1
	s_nop 1
	v_pk_mul_f32 v[66:67], v[76:77], v[76:77]
	v_add_f32_e32 v68, v74, v75
	v_add_f32_e32 v66, v68, v66
	v_add_f32_e32 v66, v66, v67
	v_add_f32_e32 v167, v167, v66

.LBB0_118:
	s_or_b64 exec, exec, s[0:1]
	v_add_u32_e32 v67, v182, v67
	ds_read_b128 v[162:165], v67
	ds_read_b128 v[94:97], v67 offset:32
	ds_read_b128 v[90:93], v67 offset:64
	ds_read_b128 v[86:89], v67 offset:96
	v_mov_b32_e32 v168, 0xff61b1e6
	s_and_saveexec_b64 s[0:1], vcc
	v_lshl_add_u32 v66, v66, 2, v250
	ds_read_b32 v168, v66
	s_or_b64 exec, exec, s[0:1]
	s_waitcnt lgkmcnt(3)
	v_mfma_f32_32x32x16_f16 v[66:81], v[98:101], v[162:165], v[2:17]
	s_waitcnt lgkmcnt(2)
	v_mfma_f32_32x32x16_f16 v[66:81], v[102:105], v[94:97], v[66:81]
	s_waitcnt lgkmcnt(1)
	v_mfma_f32_32x32x16_f16 v[66:81], v[106:109], v[90:93], v[66:81]
	s_waitcnt lgkmcnt(0)
	v_mfma_f32_32x32x16_f16 v[66:81], v[110:113], v[86:89], v[66:81]
	s_nop 11
	v_min3_f32 v254, v66, v67, v68
	v_min3_f32 v254, v254, v69, v70
	v_min3_f32 v254, v254, v71, v72
	v_min3_f32 v254, v254, v73, v74
	v_min3_f32 v254, v254, v75, v76
	v_min3_f32 v254, v254, v77, v78
	v_min3_f32 v254, v254, v79, v80
	v_min_f32_e32 v254, v254, v81
	v_cmp_lt_f32_e32 vcc, v254, v168
	s_cbranch_vccz .Lrc_skip_tile0
	v_cmp_lt_f32_e32 vcc, v66, v168
	s_and_saveexec_b64 s[0:1], vcc
	s_cbranch_execz .LBB0_125
	s_mov_b64 s[16:17], exec
	v_mbcnt_lo_u32_b32 v66, s16, 0
	v_mbcnt_hi_u32_b32 v66, s17, v66
	v_cmp_eq_u32_e32 vcc, 0, v66
	s_and_saveexec_b64 s[14:15], vcc
	s_bcnt1_i32_b64 s16, s[16:17]
	v_mov_b32_e32 v254, s16
	ds_add_rtn_u32 v254, v248, v254
	s_or_b64 exec, exec, s[14:15]
	s_waitcnt lgkmcnt(0)
	v_readfirstlane_b32 s14, v254
	s_nop 1
	v_add_u32_e32 v66, s14, v66
	v_cmp_gt_u32_e32 vcc, s20, v66
	s_and_b64 exec, exec, vcc
	v_lshl_add_u32 v66, v66, 2, v246
	ds_write_b32 v66, v179

.Lrc_skip_tile0:
	v_mfma_f32_32x32x16_f16 v[66:81], v[114:117], v[162:165], v[18:33]
	v_mfma_f32_32x32x16_f16 v[66:81], v[118:121], v[94:97], v[66:81]
	v_mfma_f32_32x32x16_f16 v[66:81], v[122:125], v[90:93], v[66:81]
	v_mfma_f32_32x32x16_f16 v[66:81], v[126:129], v[86:89], v[66:81]
	s_nop 11
	v_min3_f32 v254, v66, v67, v68
	v_min3_f32 v254, v254, v69, v70
	v_min3_f32 v254, v254, v71, v72
	v_min3_f32 v254, v254, v73, v74
	v_min3_f32 v254, v254, v75, v76
	v_min3_f32 v254, v254, v77, v78
	v_min3_f32 v254, v254, v79, v80
	v_min_f32_e32 v254, v254, v81
	v_cmp_lt_f32_e32 vcc, v254, v168
	s_cbranch_vccz .Lrc_skip_tile1
	v_cmp_lt_f32_e32 vcc, v66, v168
	s_and_saveexec_b64 s[0:1], vcc
	s_cbranch_execz .LBB0_205
	s_mov_b64 s[16:17], exec
	v_mbcnt_lo_u32_b32 v66, s16, 0
	v_mbcnt_hi_u32_b32 v66, s17, v66
	v_cmp_eq_u32_e32 vcc, 0, v66
	s_and_saveexec_b64 s[14:15], vcc
	s_bcnt1_i32_b64 s16, s[16:17]
	v_mov_b32_e32 v254, s16
	ds_add_rtn_u32 v254, v248, v254
	s_or_b64 exec, exec, s[14:15]
	s_waitcnt lgkmcnt(0)
	v_readfirstlane_b32 s14, v254
	s_nop 1
	v_add_u32_e32 v66, s14, v66
	v_cmp_gt_u32_e32 vcc, s20, v66
	s_and_b64 exec, exec, vcc
	v_lshl_add_u32 v66, v66, 2, v246
	ds_write_b32 v66, v198

.Lrc_skip_tile1:
	v_mfma_f32_32x32x16_f16 v[66:81], v[130:133], v[162:165], v[34:49]
	v_mfma_f32_32x32x16_f16 v[66:81], v[134:137], v[94:97], v[66:81]
	v_mfma_f32_32x32x16_f16 v[66:81], v[138:141], v[90:93], v[66:81]
	v_mfma_f32_32x32x16_f16 v[66:81], v[142:145], v[86:89], v[66:81]
	s_nop 11
	v_min3_f32 v254, v66, v67, v68
	v_min3_f32 v254, v254, v69, v70
	v_min3_f32 v254, v254, v71, v72
	v_min3_f32 v254, v254, v73, v74
	v_min3_f32 v254, v254, v75, v76
	v_min3_f32 v254, v254, v77, v78
	v_min3_f32 v254, v254, v79, v80
	v_min_f32_e32 v254, v254, v81
	v_cmp_lt_f32_e32 vcc, v254, v168
	s_cbranch_vccz .Lrc_skip_tile2
	v_cmp_lt_f32_e32 vcc, v66, v168
	s_and_saveexec_b64 s[0:1], vcc
	s_cbranch_execz .LBB0_285
	s_mov_b64 s[16:17], exec
	v_mbcnt_lo_u32_b32 v66, s16, 0
	v_mbcnt_hi_u32_b32 v66, s17, v66
	v_cmp_eq_u32_e32 vcc, 0, v66
	s_and_saveexec_b64 s[14:15], vcc
	s_bcnt1_i32_b64 s16, s[16:17]
	v_mov_b32_e32 v254, s16
	ds_add_rtn_u32 v254, v248, v254
	s_or_b64 exec, exec, s[14:15]
	s_waitcnt lgkmcnt(0)
	v_readfirstlane_b32 s14, v254
	s_nop 1
	v_add_u32_e32 v66, s14, v66
	v_cmp_gt_u32_e32 vcc, s20, v66
	s_and_b64 exec, exec, vcc
	v_lshl_add_u32 v66, v66, 2, v246
	ds_write_b32 v66, v214

.Lrc_skip_tile2:
	v_mfma_f32_32x32x16_f16 v[66:81], v[146:149], v[162:165], v[50:65]
	v_mfma_f32_32x32x16_f16 v[66:81], v[150:153], v[94:97], v[66:81]
	v_mfma_f32_32x32x16_f16 v[66:81], v[154:157], v[90:93], v[66:81]
	v_mfma_f32_32x32x16_f16 v[66:81], v[158:161], v[86:89], v[66:81]
	s_nop 11
	v_min3_f32 v254, v66, v67, v68
	v_min3_f32 v254, v254, v69, v70
	v_min3_f32 v254, v254, v71, v72
	v_min3_f32 v254, v254, v73, v74
	v_min3_f32 v254, v254, v75, v76
	v_min3_f32 v254, v254, v77, v78
	v_min3_f32 v254, v254, v79, v80
	v_min_f32_e32 v254, v254, v81
	v_cmp_lt_f32_e32 vcc, v254, v168
	s_cbranch_vccz .Lrc_skip_tile3
	v_cmp_lt_f32_e32 vcc, v66, v168
	s_and_saveexec_b64 s[0:1], vcc
	s_cbranch_execz .LBB0_365
	s_mov_b64 s[16:17], exec
	v_mbcnt_lo_u32_b32 v66, s16, 0
	v_mbcnt_hi_u32_b32 v66, s17, v66
	v_cmp_eq_u32_e32 vcc, 0, v66
	s_and_saveexec_b64 s[14:15], vcc
	s_bcnt1_i32_b64 s16, s[16:17]
	v_mov_b32_e32 v86, s16
	ds_add_rtn_u32 v86, v248, v86
	s_or_b64 exec, exec, s[14:15]
	s_waitcnt lgkmcnt(0)
	v_readfirstlane_b32 s14, v86
	s_nop 1
	v_add_u32_e32 v66, s14, v66
	v_cmp_gt_u32_e32 vcc, s20, v66
	s_and_b64 exec, exec, vcc
	v_lshl_add_u32 v66, v66, 2, v246
	ds_write_b32 v66, v230

.Lrc_skip_tile3:
	s_waitcnt lgkmcnt(0)
	s_barrier
	ds_read_b32 v66, v248
	s_waitcnt lgkmcnt(0)
	v_cmp_ne_u32_e32 vcc, 0, v66
	s_cbranch_vccz .LBB0_447
	v_and_b32_e32 v67, 0x70, v251
	v_min_u32_e32 v70, 0x800, v66
	v_xor_b32_e32 v66, 8, v251
	v_add_u32_e32 v67, 16, v67
	v_cmp_lt_i32_e32 vcc, v66, v67
	s_lshl_b32 s14, s25, 2
	s_add_i32 s14, s14, 0x21400
	v_cndmask_b32_e32 v66, v251, v66, vcc
	v_lshlrev_b32_e32 v71, 2, v66
	v_xor_b32_e32 v66, 4, v251
	v_cmp_lt_i32_e32 vcc, v66, v67
	s_mov_b32 s15, 0
	v_mov_b32_e32 v75, v247
	v_cndmask_b32_e32 v66, v251, v66, vcc
	v_lshlrev_b32_e32 v72, 2, v66
	v_xor_b32_e32 v66, 2, v251
	v_cmp_lt_i32_e32 vcc, v66, v67
	s_nop 1
	v_cndmask_b32_e32 v66, v251, v66, vcc
	v_lshlrev_b32_e32 v73, 2, v66
	v_xor_b32_e32 v66, 1, v251
	v_cmp_lt_i32_e32 vcc, v66, v67
	s_nop 1
	v_cndmask_b32_e32 v66, v251, v66, vcc
	v_lshlrev_b32_e32 v74, 2, v66
	s_branch .LBB0_443

.LBB0_447:
	v_mov_b32_e32 v66, 0
	s_waitcnt lgkmcnt(0)
	s_barrier
	s_and_saveexec_b64 s[0:1], s[8:9]
	s_cbranch_execz .LBB0_451
	ds_read_b64 v[66:67], v184
	s_waitcnt lgkmcnt(0)
	v_cmp_ne_u64_e32 vcc, -1, v[66:67]
	s_and_saveexec_b64 s[14:15], vcc
	s_xor_b64 s[14:15], exec, s[14:15]
	s_andn2_saveexec_b64 s[14:15], s[14:15]
	v_lshl_add_u32 v66, v253, 2, v252
	ds_read_b32 v66, v66
	s_or_b64 exec, exec, s[14:15]
	s_waitcnt lgkmcnt(0)
	v_and_b32_e32 v66, 0x3ff, v66
	v_lshl_or_b32 v67, v66, 8, v178
	global_load_dwordx4 v[68:71], v67, s[22:23]
	v_add_u32_e32 v168, s24, v253
	v_lshlrev_b64 v[72:73], 8, v[168:169]
	v_lshl_add_u64 v[72:73], v[172:173], 0, v[72:73]
	s_waitcnt vmcnt(0)
	v_pk_add_f32 v[68:69], v[68:69], v[82:83] neg_lo:[0,1] neg_hi:[0,1]
	v_pk_add_f32 v[74:75], v[70:71], v[84:85] neg_lo:[0,1] neg_hi:[0,1]
	v_pk_mul_f32 v[76:77], v[68:69], v[68:69]
	v_pk_add_f32 v[70:71], v[84:85], v[74:75]
	v_pk_mul_f32 v[74:75], v[74:75], v[74:75]
	v_add_f32_e32 v67, v76, v77
	v_add_f32_e32 v67, v67, v74
	v_add_f32_e32 v67, v67, v75
	v_pk_add_f32 v[68:69], v[82:83], v[68:69]
	v_add_f32_e32 v167, v167, v67
	global_store_dwordx4 v[72:73], v[68:71], off sc0 sc1

.LBB0_455:
	v_mbcnt_hi_u32_b32 v8, -1, v176
	v_and_b32_e32 v4, 64, v8
	v_add_u32_e32 v9, 64, v4
	v_xor_b32_e32 v4, 32, v8
	v_cmp_lt_i32_e32 vcc, v4, v9
	v_cvt_f64_f32_e32 v[2:3], v167
	v_lshlrev_b32_e32 v0, 2, v0
	v_cndmask_b32_e32 v4, v8, v4, vcc
	v_lshlrev_b32_e32 v5, 2, v4
	ds_bpermute_b32 v4, v5, v2
	ds_bpermute_b32 v5, v5, v3
	v_add_u32_e32 v6, 0x20c00, v0
	s_waitcnt lgkmcnt(0)
	s_barrier
	v_add_f64 v[2:3], v[2:3], v[4:5]
	v_xor_b32_e32 v4, 16, v8
	v_cmp_lt_i32_e32 vcc, v4, v9
	ds_read_b32 v6, v6
	s_ashr_i32 s25, s24, 31
	v_cndmask_b32_e32 v4, v8, v4, vcc
	v_lshlrev_b32_e32 v5, 2, v4
	ds_bpermute_b32 v4, v5, v2
	ds_bpermute_b32 v5, v5, v3
	s_lshl_b64 s[0:1], s[24:25], 2
	s_add_u32 s0, s12, s0
	v_mov_b32_e32 v1, 0
	s_addc_u32 s1, s13, s1
	s_waitcnt lgkmcnt(0)
	v_add_f64 v[2:3], v[2:3], v[4:5]
	v_xor_b32_e32 v4, 8, v8
	v_cmp_lt_i32_e32 vcc, v4, v9
	v_and_b32_e32 v10, 0x3ff, v6
	v_lshl_add_u64 v[6:7], s[0:1], 0, v[0:1]
	v_cndmask_b32_e32 v4, v8, v4, vcc
	v_lshlrev_b32_e32 v5, 2, v4
	ds_bpermute_b32 v4, v5, v2
	ds_bpermute_b32 v5, v5, v3
	v_xor_b32_e32 v1, 4, v8
	v_cmp_lt_i32_e32 vcc, v1, v9
	s_brev_b32 s0, 64
	v_cvt_f32_u32_e32 v11, v10
	v_cndmask_b32_e32 v1, v8, v1, vcc
	s_waitcnt lgkmcnt(0)
	v_add_f64 v[2:3], v[2:3], v[4:5]
	v_lshlrev_b32_e32 v1, 2, v1
	ds_bpermute_b32 v4, v1, v2
	ds_bpermute_b32 v5, v1, v3
	v_add_co_u32_e32 v6, vcc, s0, v6
	v_xor_b32_e32 v1, 2, v8
	s_nop 0
	v_addc_co_u32_e32 v7, vcc, 0, v7, vcc
	v_cmp_lt_i32_e32 vcc, v1, v9
	s_waitcnt lgkmcnt(0)
	v_add_f64 v[2:3], v[2:3], v[4:5]
	global_store_dword v[6:7], v11, off sc0 sc1
	v_cndmask_b32_e32 v1, v8, v1, vcc
	v_lshlrev_b32_e32 v1, 2, v1
	ds_bpermute_b32 v4, v1, v2
	ds_bpermute_b32 v5, v1, v3
	v_mov_b32_e32 v1, 0x1f400
	v_lshl_add_u32 v1, v10, 2, v1
	v_mov_b32_e32 v6, 1
	ds_add_u32 v1, v6
	v_xor_b32_e32 v1, 1, v8
	v_cmp_lt_i32_e32 vcc, v1, v9
	s_waitcnt lgkmcnt(1)
	v_add_f64 v[2:3], v[2:3], v[4:5]
	s_mov_b32 s3, 0
	v_cndmask_b32_e32 v1, v8, v1, vcc
	v_lshlrev_b32_e32 v1, 2, v1
	ds_bpermute_b32 v4, v1, v2
	ds_bpermute_b32 v5, v1, v3
	v_cmp_eq_u32_e32 vcc, 0, v166
	s_and_saveexec_b64 s[0:1], vcc
	s_cbranch_execz .LBB0_457
	s_lshl_b32 s4, s33, 3
	s_add_i32 s4, s4, 0x21d00
	s_waitcnt lgkmcnt(0)
	v_add_f64 v[2:3], v[2:3], v[4:5]
	v_mov_b32_e32 v1, s4
	ds_write_b64 v1, v[2:3]
.LBB0_457:
	s_or_b64 exec, exec, s[0:1]
	s_waitcnt lgkmcnt(0)
	s_barrier
	ds_read2st64_b32 v[2:3], v180 offset1:8
	s_lshl_b64 s[0:1], s[2:3], 12
	s_add_u32 s0, s18, s0
	s_addc_u32 s1, s19, s1
	s_waitcnt lgkmcnt(0)
	global_store_dword v0, v2, s[0:1] sc0 sc1
	global_store_dword v0, v3, s[0:1] offset:2048 sc0 sc1
	s_and_saveexec_b64 s[0:1], s[10:11]
	s_cbranch_execz .LBB0_459
	v_mov_b32_e32 v0, 0x21d00
	ds_read_b128 v[0:3], v0
	v_mov_b32_e32 v4, 0x21d10
	v_mov_b32_e32 v8, 0x21d20
	ds_read_b128 v[4:7], v4
	ds_read_b128 v[8:11], v8
	s_lshl_b64 s[0:1], s[2:3], 3
	s_waitcnt lgkmcnt(2)
	v_add_f64 v[0:1], v[0:1], 0
	v_add_f64 v[12:13], v[0:1], v[2:3]
	v_mov_b32_e32 v0, 0x21d30
	ds_read_b128 v[0:3], v0
	s_waitcnt lgkmcnt(2)
	v_add_f64 v[4:5], v[12:13], v[4:5]
	v_add_f64 v[4:5], v[4:5], v[6:7]
	s_waitcnt lgkmcnt(1)
	v_add_f64 v[4:5], v[4:5], v[8:9]
	v_add_f64 v[4:5], v[4:5], v[10:11]
	s_waitcnt lgkmcnt(0)
	v_add_f64 v[0:1], v[4:5], v[0:1]
	s_add_u32 s0, s18, s0
	v_add_f64 v[0:1], v[0:1], v[2:3]
	s_addc_u32 s1, s19, s1
	v_mov_b32_e32 v2, 0x100000
	global_store_dwordx2 v2, v[0:1], s[0:1] sc0 sc1
